# MLA loop: scalar-flag rescale gating (rare path raises an SGPR flag; the per-tile v_cmp on alpha and its VCC branch are gone)
# speedup vs baseline: 1.0047x; 1.0047x over previous
; #define SLOAD(i, j) do { const int _row = KROW(j); skn[i] = *(const bf16x8*)(Knp + (size_t)(_row + sr) * ldk + c8 * 8); sv[i] = *(const bf16x8*)(Vp + (size_t)(_row + sr) * ldv + c8 * 8); \
;         if (krw) skr[i] = *(const bf16x8*)(Krp + (size_t)(_row + sr2) * 32 + c4 * 8); } while (0)
; #define SWRITE(b, i) do { *(LAS bf16x8*)(lds + (b) * BUF + kn_st) = skn[i]; *(LAS bf16x8*)(lds + (b) * BUF + v_stw) = sv[i]; if (krw) *(LAS bf16x8*)(lds + (b) * BUF + kr_st) = skr[i]; } while (0)
; #define SWRITEO(boff, i) do { *(LAS bf16x8*)(lds + (boff) + kn_st) = skn[i]; *(LAS bf16x8*)(lds + (boff) + v_stw) = sv[i]; if (krw) *(LAS bf16x8*)(lds + (boff) + kr_st) = skr[i]; } while (0)
; #define SWAIT() asm volatile("s_waitcnt vmcnt(2)" ::: "memory")
; __device__ __forceinline__ float psm_max(const f32x16& p0, const f32x16& p1) {
;     float pmax = p0[0];
; #pragma unroll
;     for (int r = 1; r < 16; ++r) pmax = fmaxf(pmax, p0[r]);
; #pragma unroll
;     for (int r = 0; r < 16; ++r) pmax = fmaxf(pmax, p1[r]);
;     { auto rr = __builtin_amdgcn_permlane32_swap(__float_as_uint(pmax), __float_as_uint(pmax), false, false);
;       pmax = fmaxf(__uint_as_float(rr[0]), __uint_as_float(rr[1])); }
;     return pmax;
; }
; template <bool FIRST> __device__ __forceinline__ void psm_apply(f32x16& p0, f32x16& p1, float pmax, float& m_reg, f32x16& negm, float& alpha) {
;     alpha = 1.f;
;     if (FIRST || !__builtin_expect(__all(pmax <= THR2), 1)) {
;         const float delta = FIRST ? pmax : fmaxf(pmax, 0.f);
;         if (!FIRST) alpha = __builtin_amdgcn_exp2f(-delta);
;         m_reg += delta;
; #pragma unroll
;         for (int r = 0; r < 16; ++r) { p0[r] -= delta; p1[r] -= delta; negm[r] = -m_reg; }
;     }
; #pragma unroll
;     for (int r = 0; r < 16; ++r) p0[r] = EXP_PROBE ? fmaf(p0[r], 0.001f, 1.f) : __builtin_amdgcn_exp2f(p0[r]);
; }
; template <int DQK, bool FIXM> ...
;     ...
;     __syncthreads();
;     SLOAD(0, 0); asm volatile("s_waitcnt vmcnt(0)" ::: "memory"); SWRITE(0, 0);
;     SLOAD(1, 1); if (2 < NT) SLOAD(0, 2);
;     __syncthreads();
;     qkt<DQK>(pA0, pA1, lds, qr, r32, hi, negm);
;     if (FIXM) { alA = 1.f; _Pragma("unroll") for (int r = 0; r < 16; ++r) pA0[r] = __builtin_amdgcn_exp2f(pA0[r]); } else partialSM<true>(pA0, pA1, m_reg, negm, alA);
;     SWAIT(); SWRITEO(BUF, 1);
.LBB0_520:
	s_or_b64 exec, exec, s[0:1]
	v_add_u32_e32 v15, v208, v209
	s_waitcnt lgkmcnt(0)
	s_barrier
	ds_read_b128 v[34:37], v15
	ds_read_b128 v[38:41], v15 offset:4096
	s_waitcnt lgkmcnt(1)
	v_mfma_f32_32x32x16_bf16 v[50:65], v[34:37], v[166:169], 0
	v_add_u32_e32 v15, v208, v210
	ds_read_b128 v[66:69], v15
	ds_read_b128 v[70:73], v15 offset:4096
	v_add_u32_e32 v15, v208, v211
	s_waitcnt lgkmcnt(2)
	v_mfma_f32_32x32x16_bf16 v[34:49], v[38:41], v[166:169], 0
	s_waitcnt lgkmcnt(1)
	v_mfma_f32_32x32x16_bf16 v[50:65], v[66:69], v[162:165], v[50:65]
	s_waitcnt lgkmcnt(0)
	v_mfma_f32_32x32x16_bf16 v[34:49], v[70:73], v[162:165], v[34:49]
	ds_read_b128 v[66:69], v15
	ds_read_b128 v[70:73], v15 offset:4096
	v_add_u32_e32 v15, v208, v212
	s_waitcnt lgkmcnt(1)
	v_mfma_f32_32x32x16_bf16 v[50:65], v[66:69], v[158:161], v[50:65]
	s_waitcnt lgkmcnt(0)
	v_mfma_f32_32x32x16_bf16 v[34:49], v[70:73], v[158:161], v[34:49]
	ds_read_b128 v[66:69], v15
	ds_read_b128 v[70:73], v15 offset:4096
	v_add_u32_e32 v15, v218, v219
	s_waitcnt lgkmcnt(1)
	v_mfma_f32_32x32x16_bf16 v[50:65], v[66:69], v[154:157], v[50:65]
	s_waitcnt lgkmcnt(0)
	v_mfma_f32_32x32x16_bf16 v[34:49], v[70:73], v[154:157], v[34:49]
	ds_read_b128 v[66:69], v15 offset:8192
	ds_read_b128 v[70:73], v15 offset:10240
	v_add_u32_e32 v15, v218, v220
	s_waitcnt lgkmcnt(1)
	v_mfma_f32_32x32x16_bf16 v[50:65], v[66:69], v[150:153], v[50:65]
	ds_read_b128 v[66:69], v15 offset:8192
	ds_read_b128 v[74:77], v15 offset:10240
	s_waitcnt vmcnt(2)
	s_waitcnt vmcnt(3)
	ds_write_b128 v13, v[4:7] offset:20480
	s_waitcnt vmcnt(2)
	ds_write_b128 v14, v[8:11] offset:32768
	s_waitcnt lgkmcnt(3)
	v_mfma_f32_32x32x16_bf16 v[50:65], v[66:69], v[146:149], v[50:65]
	v_mfma_f32_32x32x16_bf16 v[34:49], v[70:73], v[150:153], v[34:49]
	s_nop 10
	v_max_f32_e32 v15, v51, v51
	v_max_f32_e32 v16, v50, v50
	v_max_f32_e32 v15, v16, v15
	v_max3_f32 v15, v15, v52, v53
	v_max3_f32 v15, v15, v54, v55
	v_max3_f32 v15, v15, v56, v57
	v_max3_f32 v15, v15, v58, v59
	s_waitcnt lgkmcnt(2)
	v_mfma_f32_32x32x16_bf16 v[34:49], v[74:77], v[146:149], v[34:49]
	v_max3_f32 v15, v15, v60, v61
	v_max3_f32 v15, v15, v62, v63
	v_max3_f32 v15, v15, v64, v65
	s_nop 8
	v_max3_f32 v15, v15, v34, v35
	v_max3_f32 v15, v15, v36, v37
	v_max3_f32 v15, v15, v38, v39
	v_max3_f32 v15, v15, v40, v41
	v_max3_f32 v15, v15, v42, v43
	v_max3_f32 v15, v15, v44, v45
	v_max3_f32 v15, v15, v46, v47
	v_max3_f32 v15, v15, v48, v49
	v_mov_b32_e32 v16, v15
	s_nop 1
	v_permlane32_swap_b32_e32 v15, v16
	s_and_saveexec_b64 s[0:1], s[2:3]
	ds_write_b128 v12, v[174:177] offset:28672
	s_or_b64 exec, exec, s[0:1]
	v_max_f32_e32 v4, v16, v16
	v_max_f32_e32 v5, v15, v15
	v_max_f32_e32 v4, v5, v4
	v_sub_f32_e32 v5, v50, v4
	v_sub_f32_e32 v6, v51, v4
	v_sub_f32_e32 v7, v52, v4
	v_sub_f32_e32 v8, v53, v4
	v_sub_f32_e32 v9, v54, v4
	v_sub_f32_e32 v10, v55, v4
	v_sub_f32_e32 v11, v56, v4
	v_sub_f32_e32 v12, v57, v4
	v_sub_f32_e32 v13, v58, v4
	v_sub_f32_e32 v14, v59, v4
	v_sub_f32_e32 v15, v60, v4
	v_sub_f32_e32 v16, v61, v4
	v_sub_f32_e32 v17, v62, v4
	v_sub_f32_e32 v50, v63, v4
	v_sub_f32_e32 v51, v64, v4
	v_sub_f32_e32 v52, v65, v4
	v_exp_f32_e32 v243, v5
	v_exp_f32_e32 v245, v6
	v_exp_f32_e32 v241, v7
	v_exp_f32_e32 v244, v8
	v_exp_f32_e32 v239, v9
	v_exp_f32_e32 v242, v10
	v_exp_f32_e32 v238, v11
	v_exp_f32_e32 v240, v12
	v_exp_f32_e32 v236, v13
	v_exp_f32_e32 v237, v14
	v_exp_f32_e32 v233, v15
	v_exp_f32_e32 v235, v16
	v_exp_f32_e32 v231, v17
	v_exp_f32_e32 v234, v50
	v_exp_f32_e32 v230, v51
	v_exp_f32_e32 v232, v52
	v_add_f32_e32 v224, 0, v4
	v_mov_b32_e32 v16, v3
	v_mov_b32_e32 v17, v3
	v_xor_b32_e32 v82, 0x80000000, v224
	v_sub_f32_e32 v113, v49, v4
	v_sub_f32_e32 v112, v48, v4
	v_sub_f32_e32 v111, v47, v4
	v_sub_f32_e32 v110, v46, v4
	v_sub_f32_e32 v109, v45, v4
	v_sub_f32_e32 v108, v44, v4
	v_sub_f32_e32 v107, v43, v4
	v_sub_f32_e32 v106, v42, v4
	v_sub_f32_e32 v105, v41, v4
	v_sub_f32_e32 v104, v40, v4
	v_sub_f32_e32 v103, v39, v4
	v_sub_f32_e32 v102, v38, v4
	v_sub_f32_e32 v101, v37, v4
	v_sub_f32_e32 v100, v36, v4
	v_sub_f32_e32 v99, v35, v4
	v_sub_f32_e32 v98, v34, v4
	v_lshl_add_u64 v[206:207], s[10:11], 0, v[2:3]
	s_mov_b64 s[42:43], s[10:11]
	v_mov_b32_e32 v2, v3
	v_mov_b32_e32 v4, v3
	v_mov_b32_e32 v5, v3
	v_mov_b32_e32 v6, v3
	v_mov_b32_e32 v7, v3
	v_mov_b32_e32 v8, v3
	v_mov_b32_e32 v9, v3
	v_mov_b32_e32 v10, v3
	v_mov_b32_e32 v11, v3
	v_mov_b32_e32 v12, v3
	v_mov_b32_e32 v13, v3
	v_mov_b32_e32 v14, v3
	v_mov_b32_e32 v15, v3
	v_mov_b64_e32 v[48:49], v[16:17]
	v_mov_b64_e32 v[64:65], v[16:17]
	s_ashr_i32 s9, s8, 31
	s_add_i32 s12, s31, -1
	s_mov_b32 s11, 0
	v_mov_b32_e32 v223, 0
	v_mov_b32_e32 v227, 1.0
	s_movk_i32 s13, 0x5000
	s_mov_b32 s0, 0xa000
	s_mov_b32 s35, 4
	v_readlane_b32 s44, v254, 8
	v_readlane_b32 s45, v254, 9
	s_nop 3
	s_add_u32 s44, s44, 0x1ea00000
	s_addc_u32 s45, s45, 0
	v_subrev_u32_e32 v225, s42, v206
	v_lshlrev_b32_e32 v226, 11, v221
	v_add_u32_e32 v225, v225, v226
	v_add_u32_e32 v225, 0xfff80000, v225
	v_subrev_u32_e32 v226, s44, v204
	v_lshl_add_u32 v226, v215, 6, v226
	v_mov_b64_e32 v[46:47], v[14:15]
	v_mov_b64_e32 v[44:45], v[12:13]
	v_mov_b64_e32 v[42:43], v[10:11]
	v_mov_b64_e32 v[40:41], v[8:9]
	v_mov_b64_e32 v[38:39], v[6:7]
	v_mov_b64_e32 v[36:37], v[4:5]
	v_mov_b64_e32 v[34:35], v[2:3]
	v_mov_b64_e32 v[62:63], v[14:15]
	v_mov_b64_e32 v[60:61], v[12:13]
	v_mov_b64_e32 v[58:59], v[10:11]
	v_mov_b64_e32 v[56:57], v[8:9]
	v_mov_b64_e32 v[54:55], v[6:7]
	v_mov_b64_e32 v[52:53], v[4:5]
	v_mov_b64_e32 v[50:51], v[2:3]
	v_mov_b32_e32 v83, v82
	v_mov_b32_e32 v84, v82
	v_mov_b32_e32 v85, v82
	v_mov_b32_e32 v86, v82
	v_mov_b32_e32 v87, v82
	v_mov_b32_e32 v88, v82
	v_mov_b32_e32 v89, v82
	v_mov_b32_e32 v90, v82
	v_mov_b32_e32 v91, v82
	v_mov_b32_e32 v92, v82
	v_mov_b32_e32 v93, v82
	v_mov_b32_e32 v94, v82
	v_mov_b32_e32 v95, v82
	v_mov_b32_e32 v96, v82
	v_mov_b32_e32 v97, v82
	v_add_u32_e32 v209, v201, v209
	v_add_u32_e32 v210, v201, v210
	v_add_u32_e32 v211, v201, v211
	v_add_u32_e32 v212, v201, v212
	v_add_u32_e32 v219, v217, v219
	v_add_u32_e32 v220, v217, v220
	s_mov_b32 s52, 0
	s_mov_b32 s53, 0

; #define SBAR() __builtin_amdgcn_sched_barrier(0)
; template <bool FIXM> __device__ __forceinline__ void pv_psm(f32x16& o0, f32x16& o1, unsigned vb, bf16x8 pa0, bf16x8 pa1, bf16x8 pa2, bf16x8 pa3,
;                                        f32x16& p0, f32x16& p1, float& m_reg, f32x16& negm, float& alpha) {
;     { const s16x4 l0 = tr_read<v_rd_off(0, 0, 0)>(vb), h0 = tr_read<v_rd_off(0, 0, 1)>(vb), l1 = tr_read<v_rd_off(0, 1, 0)>(vb), h1 = tr_read<v_rd_off(0, 1, 1)>(vb);
;       const s16x4 l2 = tr_read<v_rd_off(0, 2, 0)>(vb), h2 = tr_read<v_rd_off(0, 2, 1)>(vb), l3 = tr_read<v_rd_off(0, 3, 0)>(vb), h3 = tr_read<v_rd_off(0, 3, 1)>(vb);
;       float pmax = 0.f; SBAR(); if (!FIXM) pmax = psm_max(p0, p1); else { _Pragma("unroll") for (int r = 0; r < 8; ++r) p0[r] = __builtin_amdgcn_exp2f(p0[r]); } SBAR();
;       asm volatile("s_waitcnt lgkmcnt(0)" ::: "memory"); SBAR();
;       o0 = __builtin_amdgcn_mfma_f32_32x32x16_bf16(ATT_PK(l0, h0), pa0, o0, 0, 0, 0);
;       o0 = __builtin_amdgcn_mfma_f32_32x32x16_bf16(ATT_PK(l1, h1), pa1, o0, 0, 0, 0);
;       o0 = __builtin_amdgcn_mfma_f32_32x32x16_bf16(ATT_PK(l2, h2), pa2, o0, 0, 0, 0);
;       o0 = __builtin_amdgcn_mfma_f32_32x32x16_bf16(ATT_PK(l3, h3), pa3, o0, 0, 0, 0);
;       SBAR();
;       const s16x4 m0 = tr_read<v_rd_off(1, 0, 0)>(vb), n0 = tr_read<v_rd_off(1, 0, 1)>(vb), m1 = tr_read<v_rd_off(1, 1, 0)>(vb), n1 = tr_read<v_rd_off(1, 1, 1)>(vb);
;       const s16x4 m2 = tr_read<v_rd_off(1, 2, 0)>(vb), n2 = tr_read<v_rd_off(1, 2, 1)>(vb), m3 = tr_read<v_rd_off(1, 3, 0)>(vb), n3 = tr_read<v_rd_off(1, 3, 1)>(vb);
;       SBAR(); if (!FIXM) psm_apply<false>(p0, p1, pmax, m_reg, negm, alpha); else { alpha = 1.f; _Pragma("unroll") for (int r = 8; r < 16; ++r) p0[r] = __builtin_amdgcn_exp2f(p0[r]); } SBAR();
;       asm volatile("s_waitcnt lgkmcnt(0)" ::: "memory"); SBAR();
;       o1 = __builtin_amdgcn_mfma_f32_32x32x16_bf16(ATT_PK(m0, n0), pa0, o1, 0, 0, 0);
;       o1 = __builtin_amdgcn_mfma_f32_32x32x16_bf16(ATT_PK(m1, n1), pa1, o1, 0, 0, 0);
;       o1 = __builtin_amdgcn_mfma_f32_32x32x16_bf16(ATT_PK(m2, n2), pa2, o1, 0, 0, 0);
;       o1 = __builtin_amdgcn_mfma_f32_32x32x16_bf16(ATT_PK(m3, n3), pa3, o1, 0, 0, 0); }
.Lmla_a_nokr_0:
	v_exp_f32_e32 v16, v130
	v_exp_f32_e32 v234, v131
	v_mfma_f32_32x32x16_bf16 v[34:49], v[98:101], v[66:69], v[34:49]
	v_exp_f32_e32 v235, v132
	v_exp_f32_e32 v236, v133
	v_exp_f32_e32 v237, v134
	v_exp_f32_e32 v238, v135
	v_mfma_f32_32x32x16_bf16 v[34:49], v[102:105], v[70:73], v[34:49]
	v_exp_f32_e32 v239, v136
	v_exp_f32_e32 v240, v137
	v_exp_f32_e32 v241, v138
	v_exp_f32_e32 v242, v139
	v_exp_f32_e32 v243, v140
	v_mfma_f32_32x32x16_bf16 v[34:49], v[110:113], v[12:15], v[34:49]
	v_exp_f32_e32 v244, v141
	v_exp_f32_e32 v245, v142
	v_exp_f32_e32 v246, v143
	v_exp_f32_e32 v247, v144
	v_exp_f32_e32 v248, v145
	s_cmp_eq_u32 s52, 0
	s_cbranch_scc1 .LBB0_531_0
	s_mov_b32 s52, 0
	s_nop 7
	s_nop 7
	v_pk_mul_f32 v[64:65], v[64:65], v[2:3] op_sel_hi:[1,0]
	v_pk_mul_f32 v[62:63], v[62:63], v[2:3] op_sel_hi:[1,0]
	v_pk_mul_f32 v[60:61], v[60:61], v[2:3] op_sel_hi:[1,0]
	v_pk_mul_f32 v[58:59], v[58:59], v[2:3] op_sel_hi:[1,0]
	v_pk_mul_f32 v[56:57], v[56:57], v[2:3] op_sel_hi:[1,0]
	v_pk_mul_f32 v[54:55], v[54:55], v[2:3] op_sel_hi:[1,0]
	v_pk_mul_f32 v[52:53], v[52:53], v[2:3] op_sel_hi:[1,0]
	v_pk_mul_f32 v[50:51], v[50:51], v[2:3] op_sel_hi:[1,0]
	v_pk_mul_f32 v[48:49], v[48:49], v[2:3] op_sel_hi:[1,0]
	v_pk_mul_f32 v[46:47], v[46:47], v[2:3] op_sel_hi:[1,0]
	v_pk_mul_f32 v[44:45], v[44:45], v[2:3] op_sel_hi:[1,0]
	v_pk_mul_f32 v[42:43], v[42:43], v[2:3] op_sel_hi:[1,0]
	v_pk_mul_f32 v[40:41], v[40:41], v[2:3] op_sel_hi:[1,0]
	v_pk_mul_f32 v[38:39], v[38:39], v[2:3] op_sel_hi:[1,0]
	v_pk_mul_f32 v[36:37], v[36:37], v[2:3] op_sel_hi:[1,0]
	v_pk_mul_f32 v[34:35], v[34:35], v[2:3] op_sel_hi:[1,0]

; #define SBAR() __builtin_amdgcn_sched_barrier(0)
; template <bool FIXM> __device__ __forceinline__ void pv_psm(f32x16& o0, f32x16& o1, unsigned vb, bf16x8 pa0, bf16x8 pa1, bf16x8 pa2, bf16x8 pa3,
;                                        f32x16& p0, f32x16& p1, float& m_reg, f32x16& negm, float& alpha) {
;     { const s16x4 l0 = tr_read<v_rd_off(0, 0, 0)>(vb), h0 = tr_read<v_rd_off(0, 0, 1)>(vb), l1 = tr_read<v_rd_off(0, 1, 0)>(vb), h1 = tr_read<v_rd_off(0, 1, 1)>(vb);
;       const s16x4 l2 = tr_read<v_rd_off(0, 2, 0)>(vb), h2 = tr_read<v_rd_off(0, 2, 1)>(vb), l3 = tr_read<v_rd_off(0, 3, 0)>(vb), h3 = tr_read<v_rd_off(0, 3, 1)>(vb);
;       float pmax = 0.f; SBAR(); if (!FIXM) pmax = psm_max(p0, p1); else { _Pragma("unroll") for (int r = 0; r < 8; ++r) p0[r] = __builtin_amdgcn_exp2f(p0[r]); } SBAR();
;       asm volatile("s_waitcnt lgkmcnt(0)" ::: "memory"); SBAR();
;       o0 = __builtin_amdgcn_mfma_f32_32x32x16_bf16(ATT_PK(l0, h0), pa0, o0, 0, 0, 0);
;       o0 = __builtin_amdgcn_mfma_f32_32x32x16_bf16(ATT_PK(l1, h1), pa1, o0, 0, 0, 0);
;       o0 = __builtin_amdgcn_mfma_f32_32x32x16_bf16(ATT_PK(l2, h2), pa2, o0, 0, 0, 0);
;       o0 = __builtin_amdgcn_mfma_f32_32x32x16_bf16(ATT_PK(l3, h3), pa3, o0, 0, 0, 0);
;       SBAR();
;       const s16x4 m0 = tr_read<v_rd_off(1, 0, 0)>(vb), n0 = tr_read<v_rd_off(1, 0, 1)>(vb), m1 = tr_read<v_rd_off(1, 1, 0)>(vb), n1 = tr_read<v_rd_off(1, 1, 1)>(vb);
;       const s16x4 m2 = tr_read<v_rd_off(1, 2, 0)>(vb), n2 = tr_read<v_rd_off(1, 2, 1)>(vb), m3 = tr_read<v_rd_off(1, 3, 0)>(vb), n3 = tr_read<v_rd_off(1, 3, 1)>(vb);
;       SBAR(); if (!FIXM) psm_apply<false>(p0, p1, pmax, m_reg, negm, alpha); else { alpha = 1.f; _Pragma("unroll") for (int r = 8; r < 16; ++r) p0[r] = __builtin_amdgcn_exp2f(p0[r]); } SBAR();
;       asm volatile("s_waitcnt lgkmcnt(0)" ::: "memory"); SBAR();
;       o1 = __builtin_amdgcn_mfma_f32_32x32x16_bf16(ATT_PK(m0, n0), pa0, o1, 0, 0, 0);
;       o1 = __builtin_amdgcn_mfma_f32_32x32x16_bf16(ATT_PK(m1, n1), pa1, o1, 0, 0, 0);
;       o1 = __builtin_amdgcn_mfma_f32_32x32x16_bf16(ATT_PK(m2, n2), pa2, o1, 0, 0, 0);
;       o1 = __builtin_amdgcn_mfma_f32_32x32x16_bf16(ATT_PK(m3, n3), pa3, o1, 0, 0, 0); }
.Lmla_b_nokr_0:
	v_exp_f32_e32 v243, v130
	v_exp_f32_e32 v245, v131
	v_mfma_f32_32x32x16_bf16 v[34:49], v[70:73], v[230:233], v[34:49]
	v_exp_f32_e32 v241, v132
	v_exp_f32_e32 v244, v133
	v_exp_f32_e32 v239, v134
	v_exp_f32_e32 v242, v135
	v_mfma_f32_32x32x16_bf16 v[34:49], v[74:77], v[114:117], v[34:49]
	v_exp_f32_e32 v238, v136
	v_exp_f32_e32 v240, v137
	v_exp_f32_e32 v236, v138
	v_exp_f32_e32 v237, v139
	v_exp_f32_e32 v235, v141
	v_mfma_f32_32x32x16_bf16 v[34:49], v[78:81], v[118:121], v[34:49]
	v_exp_f32_e32 v234, v143
	v_exp_f32_e32 v233, v140
	v_exp_f32_e32 v231, v142
	v_exp_f32_e32 v230, v144
	v_exp_f32_e32 v232, v145
	s_cmp_eq_u32 s53, 0
	s_cbranch_scc1 .LBB0_540_0
	s_mov_b32 s53, 0
	s_nop 7
	s_nop 7
	v_pk_mul_f32 v[64:65], v[64:65], v[16:17] op_sel_hi:[1,0]
	v_pk_mul_f32 v[62:63], v[62:63], v[16:17] op_sel_hi:[1,0]
	v_pk_mul_f32 v[60:61], v[60:61], v[16:17] op_sel_hi:[1,0]
	v_pk_mul_f32 v[58:59], v[58:59], v[16:17] op_sel_hi:[1,0]
	v_pk_mul_f32 v[56:57], v[56:57], v[16:17] op_sel_hi:[1,0]
	v_pk_mul_f32 v[54:55], v[54:55], v[16:17] op_sel_hi:[1,0]
	v_pk_mul_f32 v[52:53], v[52:53], v[16:17] op_sel_hi:[1,0]
	v_pk_mul_f32 v[50:51], v[50:51], v[16:17] op_sel_hi:[1,0]
	v_pk_mul_f32 v[48:49], v[48:49], v[16:17] op_sel_hi:[1,0]
	v_pk_mul_f32 v[46:47], v[46:47], v[16:17] op_sel_hi:[1,0]
	v_pk_mul_f32 v[44:45], v[44:45], v[16:17] op_sel_hi:[1,0]
	v_pk_mul_f32 v[42:43], v[42:43], v[16:17] op_sel_hi:[1,0]
	v_pk_mul_f32 v[40:41], v[40:41], v[16:17] op_sel_hi:[1,0]
	v_pk_mul_f32 v[38:39], v[38:39], v[16:17] op_sel_hi:[1,0]
	v_pk_mul_f32 v[36:37], v[36:37], v[16:17] op_sel_hi:[1,0]
	v_pk_mul_f32 v[34:35], v[34:35], v[16:17] op_sel_hi:[1,0]

; template <bool FIRST> __device__ __forceinline__ void psm_apply(f32x16& p0, f32x16& p1, float pmax, float& m_reg, f32x16& negm, float& alpha) {
;     alpha = 1.f;
;     if (FIRST || !__builtin_expect(__all(pmax <= THR2), 1)) {
;         const float delta = FIRST ? pmax : fmaxf(pmax, 0.f);
;         if (!FIRST) alpha = __builtin_amdgcn_exp2f(-delta);
;         m_reg += delta;
; #pragma unroll
;         for (int r = 0; r < 16; ++r) { p0[r] -= delta; p1[r] -= delta; negm[r] = -m_reg; }
;     }
.LBB0_542_0:
	s_mov_b32 s52, 1
	v_mov_b32_e32 v16, v2
	s_nop 1
	v_permlane32_swap_b32_e32 v2, v16
	v_max_f32_e32 v2, v2, v16
	v_max_f32_e32 v2, v2, v2
	v_max_f32_e32 v16, 0, v2
	v_exp_f32_e64 v2, -v16
	v_add_f32_e32 v224, v224, v16
	v_xor_b32_e32 v82, 0x80000000, v224
	v_pk_add_f32 v[130:131], v[130:131], v[16:17] op_sel_hi:[1,0] neg_lo:[0,1] neg_hi:[0,1]
	v_pk_add_f32 v[132:133], v[132:133], v[16:17] op_sel_hi:[1,0] neg_lo:[0,1] neg_hi:[0,1]
	v_pk_add_f32 v[134:135], v[134:135], v[16:17] op_sel_hi:[1,0] neg_lo:[0,1] neg_hi:[0,1]
	v_pk_add_f32 v[136:137], v[136:137], v[16:17] op_sel_hi:[1,0] neg_lo:[0,1] neg_hi:[0,1]
	v_pk_add_f32 v[138:139], v[138:139], v[16:17] op_sel_hi:[1,0] neg_lo:[0,1] neg_hi:[0,1]
	v_pk_add_f32 v[140:141], v[140:141], v[16:17] op_sel_hi:[1,0] neg_lo:[0,1] neg_hi:[0,1]
	v_pk_add_f32 v[142:143], v[142:143], v[16:17] op_sel_hi:[1,0] neg_lo:[0,1] neg_hi:[0,1]
	v_pk_add_f32 v[144:145], v[144:145], v[16:17] op_sel_hi:[1,0] neg_lo:[0,1] neg_hi:[0,1]
	v_sub_f32_e32 v129, v129, v16
	v_sub_f32_e32 v128, v128, v16
	v_sub_f32_e32 v127, v127, v16
	v_sub_f32_e32 v126, v126, v16
	v_sub_f32_e32 v125, v125, v16
	v_sub_f32_e32 v124, v124, v16
	v_sub_f32_e32 v123, v123, v16
	v_sub_f32_e32 v122, v122, v16
	v_sub_f32_e32 v121, v121, v16
	v_sub_f32_e32 v120, v120, v16
	v_sub_f32_e32 v119, v119, v16
	v_sub_f32_e32 v118, v118, v16
	v_sub_f32_e32 v117, v117, v16
	v_sub_f32_e32 v116, v116, v16
	v_sub_f32_e32 v115, v115, v16
	v_sub_f32_e32 v114, v114, v16
	v_mov_b32_e32 v83, v82
	v_mov_b32_e32 v84, v82
	v_mov_b32_e32 v85, v82
	v_mov_b32_e32 v86, v82
	v_mov_b32_e32 v87, v82
	v_mov_b32_e32 v88, v82
	v_mov_b32_e32 v89, v82
	v_mov_b32_e32 v90, v82
	v_mov_b32_e32 v91, v82
	v_mov_b32_e32 v92, v82
	v_mov_b32_e32 v93, v82
	v_mov_b32_e32 v94, v82
	v_mov_b32_e32 v95, v82
	v_mov_b32_e32 v96, v82
	v_mov_b32_e32 v97, v82
	s_branch .LBB0_527_0
.LBB0_543_0:
	s_mov_b32 s53, 1
	v_mov_b32_e32 v251, v250
	s_nop 1
	v_permlane32_swap_b32_e32 v250, v251
	v_max_f32_e32 v250, v250, v251
	v_max_f32_e32 v250, v250, v250
	v_max_f32_e32 v250, 0, v250
	v_exp_f32_e64 v16, -v250
	v_add_f32_e32 v224, v224, v250
	v_xor_b32_e32 v82, 0x80000000, v224
	v_pk_add_f32 v[130:131], v[130:131], v[250:251] op_sel_hi:[1,0] neg_lo:[0,1] neg_hi:[0,1]
	v_pk_add_f32 v[132:133], v[132:133], v[250:251] op_sel_hi:[1,0] neg_lo:[0,1] neg_hi:[0,1]
	v_pk_add_f32 v[134:135], v[134:135], v[250:251] op_sel_hi:[1,0] neg_lo:[0,1] neg_hi:[0,1]
	v_pk_add_f32 v[136:137], v[136:137], v[250:251] op_sel_hi:[1,0] neg_lo:[0,1] neg_hi:[0,1]
	v_pk_add_f32 v[138:139], v[138:139], v[250:251] op_sel_hi:[1,0] neg_lo:[0,1] neg_hi:[0,1]
	v_pk_add_f32 v[140:141], v[140:141], v[250:251] op_sel_hi:[1,0] neg_lo:[0,1] neg_hi:[0,1]
	v_pk_add_f32 v[142:143], v[142:143], v[250:251] op_sel_hi:[1,0] neg_lo:[0,1] neg_hi:[0,1]
	v_pk_add_f32 v[144:145], v[144:145], v[250:251] op_sel_hi:[1,0] neg_lo:[0,1] neg_hi:[0,1]
	v_sub_f32_e32 v113, v113, v250
	v_sub_f32_e32 v112, v112, v250
	v_sub_f32_e32 v111, v111, v250
	v_sub_f32_e32 v110, v110, v250
	v_sub_f32_e32 v109, v109, v250
	v_sub_f32_e32 v108, v108, v250
	v_sub_f32_e32 v107, v107, v250
	v_sub_f32_e32 v106, v106, v250
	v_sub_f32_e32 v105, v105, v250
	v_sub_f32_e32 v104, v104, v250
	v_sub_f32_e32 v103, v103, v250
	v_sub_f32_e32 v102, v102, v250
	v_sub_f32_e32 v101, v101, v250
	v_sub_f32_e32 v100, v100, v250
	v_sub_f32_e32 v99, v99, v250
	v_sub_f32_e32 v98, v98, v250
	v_mov_b32_e32 v83, v82
	v_mov_b32_e32 v84, v82
	v_mov_b32_e32 v85, v82
	v_mov_b32_e32 v86, v82
	v_mov_b32_e32 v87, v82
	v_mov_b32_e32 v88, v82
	v_mov_b32_e32 v89, v82
	v_mov_b32_e32 v90, v82
	v_mov_b32_e32 v91, v82
	v_mov_b32_e32 v92, v82
	v_mov_b32_e32 v93, v82
	v_mov_b32_e32 v94, v82
	v_mov_b32_e32 v95, v82
	v_mov_b32_e32 v96, v82
	v_mov_b32_e32 v97, v82
	s_branch .LBB0_536_0
